# speedup vs baseline: 1.0038x; 1.0038x over previous
_Z11gram_kernelPKfPKiS0_S0_S0_S0_S0_S0_S0_S0_S0_Pf:
	s_load_dwordx4 s[24:27], s[0:1], 0x0
	s_load_dwordx2 s[28:29], s[0:1], 0x40
	s_load_dwordx4 s[20:23], s[0:1], 0x30
	s_load_dwordx2 s[10:11], s[0:1], 0x58
	s_load_dwordx2 s[44:45], s[0:1], 0x20
	s_load_dwordx2 s[68:69], s[0:1], 0x10
	s_load_dwordx2 s[60:61], s[0:1], 0x18
	s_load_dwordx2 s[62:63], s[0:1], 0x28
	s_load_dwordx2 s[64:65], s[0:1], 0x48
	s_load_dwordx2 s[66:67], s[0:1], 0x50
	s_ashr_i32 s30, s2, 1
	v_mov_b32_e32 v11, 0
	s_ashr_i32 s31, s30, 31
	s_lshl_b32 s46, s30, 11
	s_lshl_b32 s3, s2, 10
	s_ashr_i32 s47, s46, 31
	s_and_b32 s33, s3, 0x400
	v_lshlrev_b32_e32 v46, 2, v0
	v_mov_b32_e32 v47, 0
	v_lshlrev_b32_e32 v212, 1, v0
	v_mov_b32_e32 v213, v47
	v_lshrrev_b32_e32 v219, 6, v0
	v_bfe_u32 v214, v0, 5, 1
	v_and_b32_e32 v220, 31, v0
	s_or_b32 s3, s46, s33
	v_lshlrev_b32_e32 v216, 4, v219
	v_lshlrev_b32_e32 v221, 3, v214
	v_or3_b32 v1, s3, v216, v221
	v_lshlrev_b32_e32 v232, 4, v220
	v_and_b32_e32 v218, 63, v0
	s_mov_b32 s39, 0x20000
	s_brev_b32 s38, 16
	v_lshl_or_b32 v180, v1, 9, v232
	v_add_u32_e32 v1, 0x10000, v180
	s_lshl_b64 s[4:5], s[46:47], 2
	s_lshl_b32 s3, s33, 2
	s_lshl_b64 s[6:7], s[30:31], 14
	s_waitcnt lgkmcnt(0)
	s_add_u32 s48, s20, s6
	s_addc_u32 s49, s21, s7
	s_mov_b64 s[36:37], s[24:25]
	s_and_b32 s37, s37, 0xffff
	s_add_u32 s26, s26, s4
	s_addc_u32 s27, s27, s5
	s_add_u32 s26, s26, s3
	s_addc_u32 s27, s27, 0
	v_lshl_add_u64 v[32:33], v[212:213], 2, s[26:27]
	global_load_dwordx2 v[32:33], v[32:33], off
	buffer_load_dwordx4 v[34:37], v180, s[36:39], 0 offen nt
	buffer_load_dwordx4 v[38:41], v180, s[36:39], 0 offen offset:512 nt
	buffer_load_dwordx4 v[42:45], v180, s[36:39], 0 offen offset:1024 nt
	buffer_load_dwordx4 v[96:99], v180, s[36:39], 0 offen offset:1536 nt
	buffer_load_dwordx4 v[100:103], v180, s[36:39], 0 offen offset:2048 nt
	buffer_load_dwordx4 v[104:107], v180, s[36:39], 0 offen offset:2560 nt
	buffer_load_dwordx4 v[108:111], v180, s[36:39], 0 offen offset:3072 nt
	buffer_load_dwordx4 v[112:115], v180, s[36:39], 0 offen offset:3584 nt
	global_load_dword v250, v47, s[22:23]
	global_load_dword v250, v47, s[28:29]
	global_load_dword v250, v47, s[68:69]
	global_load_dword v250, v47, s[44:45]
	global_load_dword v250, v47, s[48:49]
	global_load_dword v250, v47, s[60:61]
	global_load_dword v250, v47, s[62:63]
	global_load_dword v250, v47, s[64:65]
	global_load_dword v250, v47, s[66:67]
	buffer_load_dwordx4 v[116:119], v1, s[36:39], 0 offen nt
	buffer_load_dwordx4 v[120:123], v1, s[36:39], 0 offen offset:512 nt
	buffer_load_dwordx4 v[124:127], v1, s[36:39], 0 offen offset:1024 nt
	buffer_load_dwordx4 v[128:131], v1, s[36:39], 0 offen offset:1536 nt
	buffer_load_dwordx4 v[132:135], v1, s[36:39], 0 offen offset:2048 nt
	buffer_load_dwordx4 v[136:139], v1, s[36:39], 0 offen offset:2560 nt
	buffer_load_dwordx4 v[140:143], v1, s[36:39], 0 offen offset:3072 nt
	buffer_load_dwordx4 v[144:147], v1, s[36:39], 0 offen offset:3584 nt
	s_branch .Lpad_a
.Ltop_resume:
	s_movk_i32 s3, 0x160
	v_cmp_gt_u32_e32 vcc, s3, v0
	s_mov_b32 s3, 0x10000
	v_lshrrev_b32_e32 v227, 5, v0
	v_and_b32_e32 v228, 0x7c, v46
	v_add_u32_e32 v2, 0x200, v0
	v_lshrrev_b32_e32 v229, 5, v2
	v_mul_u32_u24_e32 v246, 0x110, v227
	v_lshl_add_u32 v246, v220, 3, v246
	v_add_u32_e32 v246, 0x10000, v246
	v_lshlrev_b32_e32 v247, 2, v46
	s_waitcnt vmcnt(25)
	v_cmp_ne_u32_e64 s[6:7], 0, v32
	v_cmp_ne_u32_e64 s[4:5], 0, v33
	v_cmp_eq_u32_e64 s[8:9], 0, v218
	s_nop 0
	s_and_saveexec_b64 s[12:13], s[8:9]
	s_cbranch_execz .LBB0_6
	s_bcnt1_i32_b64 s6, s[6:7]
	s_bcnt1_i32_b64 s4, s[4:5]
	v_mov_b32_e32 v1, 0x21100
	s_add_i32 s4, s4, s6
	v_lshl_add_u32 v1, v219, 2, v1
	v_mov_b32_e32 v2, s4
	ds_write_b32 v1, v2

.LBB0_32:
	s_or_b64 exec, exec, s[20:21]
	s_mov_b32 s40, s22
	s_mov_b32 s30, s42
	s_mov_b32 s31, s43
	buffer_load_dwordx4 v[148:151], v1, s[40:43], 0 offen nt
	buffer_load_dwordx4 v[152:155], v1, s[40:43], 0 offen offset:512 nt
	buffer_load_dwordx4 v[116:119], v1, s[28:31], 0 offen nt
	buffer_load_dwordx4 v[120:123], v1, s[28:31], 0 offen offset:512 nt
	buffer_load_dwordx4 v[164:167], v1, s[40:43], 0 offen offset:1024 nt
	buffer_load_dwordx4 v[156:159], v1, s[40:43], 0 offen offset:1536 nt
	buffer_load_dwordx4 v[124:127], v1, s[28:31], 0 offen offset:1024 nt
	buffer_load_dwordx4 v[128:131], v1, s[28:31], 0 offen offset:1536 nt
	buffer_load_dwordx4 v[160:163], v1, s[40:43], 0 offen offset:2048 nt
	buffer_load_dwordx4 v[168:171], v1, s[40:43], 0 offen offset:2560 nt
	buffer_load_dwordx4 v[132:135], v1, s[28:31], 0 offen offset:2048 nt
	buffer_load_dwordx4 v[136:139], v1, s[28:31], 0 offen offset:2560 nt
	buffer_load_dwordx4 v[172:175], v1, s[40:43], 0 offen offset:3072 nt
	buffer_load_dwordx4 v[176:179], v1, s[40:43], 0 offen offset:3584 nt
	buffer_load_dwordx4 v[140:143], v1, s[28:31], 0 offen offset:3072 nt
	buffer_load_dwordx4 v[144:147], v1, s[28:31], 0 offen offset:3584 nt
	s_branch .LBB0_33
.Lpad_a:
	s_branch .Lpad_b

.LBB0_47:
	s_or_b64 exec, exec, s[0:1]
	ds_bpermute_b32 v16, v102, v23
	v_and_or_b32 v17, v101, 64, v22
	v_lshlrev_b32_e32 v31, 2, v17
	s_waitcnt lgkmcnt(0)
	v_add_f32_e32 v32, v23, v16
	ds_bpermute_b32 v16, v31, v32
	ds_bpermute_b32 v17, v31, v32 offset:4
	ds_bpermute_b32 v18, v31, v32 offset:8
	ds_bpermute_b32 v19, v31, v32 offset:12
	ds_bpermute_b32 v20, v31, v32 offset:32
	ds_bpermute_b32 v21, v31, v32 offset:36
	ds_bpermute_b32 v22, v31, v32 offset:40
	ds_bpermute_b32 v23, v31, v32 offset:44
	ds_bpermute_b32 v24, v31, v32 offset:64
	ds_bpermute_b32 v25, v31, v32 offset:68
	ds_bpermute_b32 v26, v31, v32 offset:72
	ds_bpermute_b32 v28, v31, v32 offset:96
	ds_bpermute_b32 v29, v31, v32 offset:100
	ds_bpermute_b32 v27, v31, v32 offset:76
	ds_bpermute_b32 v30, v31, v32 offset:104
	v_or_b32_e32 v31, 0x6c, v31
	ds_bpermute_b32 v31, v31, v32
	s_waitcnt lgkmcnt(3)
	v_pk_add_f32 v[12:13], v[12:13], v[28:29]
	s_waitcnt lgkmcnt(2)
	v_pk_add_f32 v[10:11], v[10:11], v[26:27]
	v_pk_add_f32 v[8:9], v[8:9], v[24:25]
	v_pk_add_f32 v[6:7], v[6:7], v[22:23]
	v_pk_add_f32 v[4:5], v[4:5], v[20:21]
	v_pk_add_f32 v[2:3], v[2:3], v[18:19]
	v_pk_add_f32 v[0:1], v[0:1], v[16:17]
	s_waitcnt lgkmcnt(0)
	v_pk_add_f32 v[14:15], v[14:15], v[30:31]
	s_branch .LBB0_48
